# best config with converter throttle s_sleep 40 instead of 30
# baseline (speedup 1.0000x reference)
; DI s16x4 tr16(const LAS unsigned char* p) { return __builtin_bit_cast(s16x4, __builtin_amdgcn_ds_read_tr16_b64_v4i16((LAS v4i16_t*)p)); }
; #define LDS_WAIT() asm volatile("s_waitcnt lgkmcnt(0)" ::: "memory")
; #define P0S_F8(lo, hi) pk4_fp8m(__uint_as_float((lo) << 16), __uint_as_float((lo) & 0xffff0000u), __uint_as_float((hi) << 16), __uint_as_float((hi) & 0xffff0000u))
; DI unsigned pk4_fp8m(float a, float b, float c, float d) {
;     a = __builtin_amdgcn_fmed3f(a, -448.f, 448.f); b = __builtin_amdgcn_fmed3f(b, -448.f, 448.f); c = __builtin_amdgcn_fmed3f(c, -448.f, 448.f); d = __builtin_amdgcn_fmed3f(d, -448.f, 448.f);
;     int v = __builtin_amdgcn_cvt_pk_fp8_f32(a, b, 0, false); v = __builtin_amdgcn_cvt_pk_fp8_f32(c, d, v, true); return (unsigned)v; }
; template <int MODE>
; DI void p0_strip_fp8(const float* W, int ld, unsigned char* WT, int K, int n0, LAS unsigned char* img, int lane) {
;     ...
;         LDS_WAIT();
; #pragma unroll 2
;         for (int nb = 0; nb < 8; ++nb) {
;             const s16x4 t0 = tr16(img + rb[0] + 32 * (nb ^ cx[0])), t1 = tr16(img + rb[1] + 32 * (nb ^ cx[1])), t2 = tr16(img + rb[2] + 32 * (nb ^ cx[2])), t3 = tr16(img + rb[3] + 32 * (nb ^ cx[3]));
;             const u32x2 f0 = __builtin_bit_cast(u32x2, t0), f1 = __builtin_bit_cast(u32x2, t1), f2 = __builtin_bit_cast(u32x2, t2), f3 = __builtin_bit_cast(u32x2, t3);
;             u32x4 o; o.x = P0S_F8(f0.x, f0.y); o.y = P0S_F8(f1.x, f1.y); o.z = P0S_F8(f2.x, f2.y); o.w = P0S_F8(f3.x, f3.y);
;             *(u32x4*)(WT + (size_t)(unsigned)orow[nb] + 64 * kb) = o; }
;         LDS_WAIT();
;     }
.LBB0_281:
	v_xor_b32_e32 v82, s2, v150
	v_xor_b32_e32 v83, s2, v151
	s_cmp_eq_u32 s2, 1
	v_lshlrev_b32_e32 v82, 5, v82
	v_lshlrev_b32_e32 v83, 5, v83
	s_cselect_b64 vcc, -1, 0
	s_cmp_eq_u32 s2, 2
	v_cndmask_b32_e32 v84, v2, v1, vcc
	v_add_u32_e32 v85, v152, v82
	v_add_u32_e32 v86, v153, v82
	v_add_u32_e32 v87, v152, v83
	v_add_u32_e32 v88, v153, v83
	s_cselect_b64 vcc, -1, 0
	s_cmp_eq_u32 s2, 3
	v_cndmask_b32_e32 v90, v84, v4, vcc
	ds_read_b64_tr_b16 v[82:83], v85
	ds_read_b64_tr_b16 v[84:85], v86 offset:1024
	ds_read_b64_tr_b16 v[86:87], v87 offset:2048
	ds_read_b64_tr_b16 v[88:89], v88 offset:3072
	s_cselect_b64 vcc, -1, 0
	s_cmp_eq_u32 s2, 4
	v_cndmask_b32_e32 v90, v90, v3, vcc
	s_cselect_b64 vcc, -1, 0
	s_cmp_eq_u32 s2, 5
	v_cndmask_b32_e32 v90, v90, v6, vcc
	s_cselect_b64 vcc, -1, 0
	s_cmp_eq_u32 s2, 6
	v_cndmask_b32_e32 v90, v90, v5, vcc
	s_cselect_b64 vcc, -1, 0
	s_cmp_eq_u32 s2, 7
	v_cndmask_b32_e32 v90, v90, v8, vcc
	s_cselect_b64 vcc, -1, 0
	s_add_i32 s63, s2, 1
	s_waitcnt lgkmcnt(3)
	v_lshlrev_b32_e32 v91, 16, v82
	v_and_b32_e32 v82, 0xffff0000, v82
	v_lshlrev_b32_e32 v92, 16, v83
	v_and_b32_e32 v83, 0xffff0000, v83
	s_waitcnt lgkmcnt(2)
	v_lshlrev_b32_e32 v93, 16, v84
	v_and_b32_e32 v84, 0xffff0000, v84
	v_lshlrev_b32_e32 v94, 16, v85
	v_and_b32_e32 v85, 0xffff0000, v85
	s_waitcnt lgkmcnt(1)
	v_lshlrev_b32_e32 v95, 16, v86
	v_and_b32_e32 v86, 0xffff0000, v86
	v_lshlrev_b32_e32 v96, 16, v87
	v_and_b32_e32 v87, 0xffff0000, v87
	s_waitcnt lgkmcnt(0)
	v_lshlrev_b32_e32 v97, 16, v88
	v_and_b32_e32 v88, 0xffff0000, v88
	v_lshlrev_b32_e32 v98, 16, v89
	v_and_b32_e32 v89, 0xffff0000, v89
	v_xor_b32_e32 v99, s63, v150
	v_xor_b32_e32 v100, s63, v151
	v_mov_b32_e32 v74, 0
	v_mov_b32_e32 v75, 0
	v_mov_b32_e32 v76, 0
	v_mov_b32_e32 v77, 0
	v_med3_f32 v91, v91, s52, v163
	v_med3_f32 v82, v82, s52, v163
	v_med3_f32 v101, v83, s52, v163
	v_med3_f32 v83, v93, s52, v163
	v_med3_f32 v84, v84, s52, v163
	v_med3_f32 v93, v94, s52, v163
	v_med3_f32 v94, v85, s52, v163
	v_med3_f32 v85, v95, s52, v163
	v_med3_f32 v86, v86, s52, v163
	v_med3_f32 v95, v96, s52, v163
	v_med3_f32 v96, v87, s52, v163
	v_med3_f32 v87, v97, s52, v163
	v_med3_f32 v88, v88, s52, v163
	v_med3_f32 v97, v98, s52, v163
	v_med3_f32 v98, v89, s52, v163
	v_lshlrev_b32_e32 v89, 5, v99
	v_lshlrev_b32_e32 v99, 5, v100
	v_cvt_pk_fp8_f32 v74, v91, v82
	v_cvt_pk_fp8_f32 v75, v83, v84
	v_cvt_pk_fp8_f32 v76, v85, v86
	v_cvt_pk_fp8_f32 v77, v87, v88
	v_add_u32_e32 v82, v152, v89
	v_add_u32_e32 v84, v153, v89
	v_add_u32_e32 v86, v152, v99
	v_add_u32_e32 v88, v153, v99
	ds_read_b64_tr_b16 v[82:83], v82
	ds_read_b64_tr_b16 v[84:85], v84 offset:1024
	ds_read_b64_tr_b16 v[86:87], v86 offset:2048
	ds_read_b64_tr_b16 v[88:89], v88 offset:3072
	v_med3_f32 v92, v92, s52, v163
	s_cmp_eq_u32 s63, 1
	v_cvt_pk_fp8_f32 v74, v92, v101 op_sel:[0,0,1]
	v_cvt_pk_fp8_f32 v75, v93, v94 op_sel:[0,0,1]
	v_cvt_pk_fp8_f32 v76, v95, v96 op_sel:[0,0,1]
	v_cvt_pk_fp8_f32 v77, v97, v98 op_sel:[0,0,1]
	s_waitcnt lgkmcnt(3)
	v_lshlrev_b32_e32 v92, 16, v82
	v_and_b32_e32 v82, 0xffff0000, v82
	s_waitcnt lgkmcnt(2)
	v_lshlrev_b32_e32 v94, 16, v84
	v_and_b32_e32 v84, 0xffff0000, v84
	s_waitcnt lgkmcnt(1)
	v_lshlrev_b32_e32 v96, 16, v86
	v_and_b32_e32 v86, 0xffff0000, v86
	s_waitcnt lgkmcnt(0)
	v_lshlrev_b32_e32 v98, 16, v88
	v_and_b32_e32 v88, 0xffff0000, v88
	v_mov_b32_e32 v78, 0
	v_mov_b32_e32 v79, 0
	v_mov_b32_e32 v80, 0
	v_mov_b32_e32 v81, 0
	v_cndmask_b32_e32 v90, v90, v7, vcc
	s_cselect_b64 vcc, -1, 0
	s_cmp_eq_u32 s63, 2
	v_med3_f32 v92, v92, s52, v163
	v_med3_f32 v82, v82, s52, v163
	v_med3_f32 v94, v94, s52, v163
	v_med3_f32 v84, v84, s52, v163
	v_med3_f32 v96, v96, s52, v163
	v_med3_f32 v86, v86, s52, v163
	v_med3_f32 v98, v98, s52, v163
	v_med3_f32 v88, v88, s52, v163
	v_cndmask_b32_e32 v100, v2, v1, vcc
	s_cselect_b64 vcc, -1, 0
	s_cmp_eq_u32 s63, 3
	v_cvt_pk_fp8_f32 v78, v92, v82
	v_cvt_pk_fp8_f32 v79, v94, v84
	v_cvt_pk_fp8_f32 v80, v96, v86
	v_cvt_pk_fp8_f32 v81, v98, v88
	v_cndmask_b32_e32 v91, v100, v4, vcc
	s_cselect_b64 vcc, -1, 0
	s_cmp_eq_u32 s63, 4
	v_cndmask_b32_e32 v91, v91, v3, vcc
	s_cselect_b64 vcc, -1, 0
	s_cmp_eq_u32 s63, 5
	v_lshlrev_b32_e32 v93, 16, v83
	v_and_b32_e32 v83, 0xffff0000, v83
	v_lshlrev_b32_e32 v95, 16, v85
	v_and_b32_e32 v85, 0xffff0000, v85
	v_lshlrev_b32_e32 v97, 16, v87
	v_and_b32_e32 v87, 0xffff0000, v87
	v_lshlrev_b32_e32 v99, 16, v89
	v_and_b32_e32 v89, 0xffff0000, v89
	v_cndmask_b32_e32 v91, v91, v6, vcc
	s_cselect_b64 vcc, -1, 0
	s_cmp_eq_u32 s63, 6
	v_med3_f32 v93, v93, s52, v163
	v_med3_f32 v83, v83, s52, v163
	v_med3_f32 v95, v95, s52, v163
	v_med3_f32 v85, v85, s52, v163
	v_med3_f32 v97, v97, s52, v163
	v_med3_f32 v87, v87, s52, v163
	v_med3_f32 v99, v99, s52, v163
	v_med3_f32 v89, v89, s52, v163
	v_cndmask_b32_e32 v91, v91, v5, vcc
	s_cselect_b64 vcc, -1, 0
	s_cmp_eq_u32 s63, 7
	v_cvt_pk_fp8_f32 v78, v93, v83 op_sel:[0,0,1]
	v_cvt_pk_fp8_f32 v79, v95, v85 op_sel:[0,0,1]
	v_cvt_pk_fp8_f32 v80, v97, v87 op_sel:[0,0,1]
	v_cvt_pk_fp8_f32 v81, v99, v89 op_sel:[0,0,1]
	v_cndmask_b32_e32 v91, v91, v8, vcc
	s_cselect_b64 vcc, -1, 0
	s_add_i32 s2, s2, 2
	s_cmp_eq_u32 s2, 8
	v_cndmask_b32_e32 v91, v91, v7, vcc
	global_store_dwordx4 v90, v[74:77], s[6:7] nt
	global_store_dwordx4 v91, v[78:81], s[6:7] nt
	s_cbranch_scc0 .LBB0_281
	s_sleep 40
	s_waitcnt lgkmcnt(0)
	s_add_i32 s62, s62, 1
	s_cmp_eq_u32 s62, 32
	s_cbranch_scc0 .LBB0_278
	s_mov_b64 s[0:1], 0

; DI s16x4 tr16(const LAS unsigned char* p) { return __builtin_bit_cast(s16x4, __builtin_amdgcn_ds_read_tr16_b64_v4i16((LAS v4i16_t*)p)); }
; #define LDS_WAIT() asm volatile("s_waitcnt lgkmcnt(0)" ::: "memory")
; #define P0S_F8(lo, hi) pk4_fp8m(__uint_as_float((lo) << 16), __uint_as_float((lo) & 0xffff0000u), __uint_as_float((hi) << 16), __uint_as_float((hi) & 0xffff0000u))
; DI unsigned pk4_fp8m(float a, float b, float c, float d) {
;     a = __builtin_amdgcn_fmed3f(a, -448.f, 448.f); b = __builtin_amdgcn_fmed3f(b, -448.f, 448.f); c = __builtin_amdgcn_fmed3f(c, -448.f, 448.f); d = __builtin_amdgcn_fmed3f(d, -448.f, 448.f);
;     int v = __builtin_amdgcn_cvt_pk_fp8_f32(a, b, 0, false); v = __builtin_amdgcn_cvt_pk_fp8_f32(c, d, v, true); return (unsigned)v; }
; template <int MODE>
; DI void p0_strip_fp8(const float* W, int ld, unsigned char* WT, int K, int n0, LAS unsigned char* img, int lane) {
;     ...
;         LDS_WAIT();
; #pragma unroll 2
;         for (int nb = 0; nb < 8; ++nb) {
;             const s16x4 t0 = tr16(img + rb[0] + 32 * (nb ^ cx[0])), t1 = tr16(img + rb[1] + 32 * (nb ^ cx[1])), t2 = tr16(img + rb[2] + 32 * (nb ^ cx[2])), t3 = tr16(img + rb[3] + 32 * (nb ^ cx[3]));
;             const u32x2 f0 = __builtin_bit_cast(u32x2, t0), f1 = __builtin_bit_cast(u32x2, t1), f2 = __builtin_bit_cast(u32x2, t2), f3 = __builtin_bit_cast(u32x2, t3);
;             u32x4 o; o.x = P0S_F8(f0.x, f0.y); o.y = P0S_F8(f1.x, f1.y); o.z = P0S_F8(f2.x, f2.y); o.w = P0S_F8(f3.x, f3.y);
;             *(u32x4*)(WT + (size_t)(unsigned)orow[nb] + 64 * kb) = o; }
;         LDS_WAIT();
;     }
.LBB0_289:
	v_xor_b32_e32 v82, s2, v150
	v_xor_b32_e32 v83, s2, v151
	s_cmp_eq_u32 s2, 1
	v_lshlrev_b32_e32 v82, 5, v82
	v_lshlrev_b32_e32 v83, 5, v83
	s_cselect_b64 vcc, -1, 0
	s_cmp_eq_u32 s2, 2
	v_cndmask_b32_e32 v84, v2, v1, vcc
	v_add_u32_e32 v85, v152, v82
	v_add_u32_e32 v86, v153, v82
	v_add_u32_e32 v87, v152, v83
	v_add_u32_e32 v88, v153, v83
	s_cselect_b64 vcc, -1, 0
	s_cmp_eq_u32 s2, 3
	v_cndmask_b32_e32 v90, v84, v4, vcc
	ds_read_b64_tr_b16 v[82:83], v85
	ds_read_b64_tr_b16 v[84:85], v86 offset:1024
	ds_read_b64_tr_b16 v[86:87], v87 offset:2048
	ds_read_b64_tr_b16 v[88:89], v88 offset:3072
	s_cselect_b64 vcc, -1, 0
	s_cmp_eq_u32 s2, 4
	v_cndmask_b32_e32 v90, v90, v3, vcc
	s_cselect_b64 vcc, -1, 0
	s_cmp_eq_u32 s2, 5
	v_cndmask_b32_e32 v90, v90, v6, vcc
	s_cselect_b64 vcc, -1, 0
	s_cmp_eq_u32 s2, 6
	v_cndmask_b32_e32 v90, v90, v5, vcc
	s_cselect_b64 vcc, -1, 0
	s_cmp_eq_u32 s2, 7
	v_cndmask_b32_e32 v90, v90, v8, vcc
	s_cselect_b64 vcc, -1, 0
	s_add_i32 s62, s2, 1
	s_waitcnt lgkmcnt(3)
	v_lshlrev_b32_e32 v91, 16, v82
	v_and_b32_e32 v82, 0xffff0000, v82
	v_lshlrev_b32_e32 v92, 16, v83
	v_and_b32_e32 v83, 0xffff0000, v83
	s_waitcnt lgkmcnt(2)
	v_lshlrev_b32_e32 v93, 16, v84
	v_and_b32_e32 v84, 0xffff0000, v84
	v_lshlrev_b32_e32 v94, 16, v85
	v_and_b32_e32 v85, 0xffff0000, v85
	s_waitcnt lgkmcnt(1)
	v_lshlrev_b32_e32 v95, 16, v86
	v_and_b32_e32 v86, 0xffff0000, v86
	v_lshlrev_b32_e32 v96, 16, v87
	v_and_b32_e32 v87, 0xffff0000, v87
	s_waitcnt lgkmcnt(0)
	v_lshlrev_b32_e32 v97, 16, v88
	v_and_b32_e32 v88, 0xffff0000, v88
	v_lshlrev_b32_e32 v98, 16, v89
	v_and_b32_e32 v89, 0xffff0000, v89
	v_xor_b32_e32 v99, s62, v150
	v_xor_b32_e32 v100, s62, v151
	v_mov_b32_e32 v74, 0
	v_mov_b32_e32 v75, 0
	v_mov_b32_e32 v76, 0
	v_mov_b32_e32 v77, 0
	v_med3_f32 v91, v91, s52, v163
	v_med3_f32 v82, v82, s52, v163
	v_med3_f32 v101, v83, s52, v163
	v_med3_f32 v83, v93, s52, v163
	v_med3_f32 v84, v84, s52, v163
	v_med3_f32 v93, v94, s52, v163
	v_med3_f32 v94, v85, s52, v163
	v_med3_f32 v85, v95, s52, v163
	v_med3_f32 v86, v86, s52, v163
	v_med3_f32 v95, v96, s52, v163
	v_med3_f32 v96, v87, s52, v163
	v_med3_f32 v87, v97, s52, v163
	v_med3_f32 v88, v88, s52, v163
	v_med3_f32 v97, v98, s52, v163
	v_med3_f32 v98, v89, s52, v163
	v_lshlrev_b32_e32 v89, 5, v99
	v_lshlrev_b32_e32 v99, 5, v100
	v_cvt_pk_fp8_f32 v74, v91, v82
	v_cvt_pk_fp8_f32 v75, v83, v84
	v_cvt_pk_fp8_f32 v76, v85, v86
	v_cvt_pk_fp8_f32 v77, v87, v88
	v_add_u32_e32 v82, v152, v89
	v_add_u32_e32 v84, v153, v89
	v_add_u32_e32 v86, v152, v99
	v_add_u32_e32 v88, v153, v99
	ds_read_b64_tr_b16 v[82:83], v82
	ds_read_b64_tr_b16 v[84:85], v84 offset:1024
	ds_read_b64_tr_b16 v[86:87], v86 offset:2048
	ds_read_b64_tr_b16 v[88:89], v88 offset:3072
	v_med3_f32 v92, v92, s52, v163
	s_cmp_eq_u32 s62, 1
	v_cvt_pk_fp8_f32 v74, v92, v101 op_sel:[0,0,1]
	v_cvt_pk_fp8_f32 v75, v93, v94 op_sel:[0,0,1]
	v_cvt_pk_fp8_f32 v76, v95, v96 op_sel:[0,0,1]
	v_cvt_pk_fp8_f32 v77, v97, v98 op_sel:[0,0,1]
	s_waitcnt lgkmcnt(3)
	v_lshlrev_b32_e32 v92, 16, v82
	v_and_b32_e32 v82, 0xffff0000, v82
	s_waitcnt lgkmcnt(2)
	v_lshlrev_b32_e32 v94, 16, v84
	v_and_b32_e32 v84, 0xffff0000, v84
	s_waitcnt lgkmcnt(1)
	v_lshlrev_b32_e32 v96, 16, v86
	v_and_b32_e32 v86, 0xffff0000, v86
	s_waitcnt lgkmcnt(0)
	v_lshlrev_b32_e32 v98, 16, v88
	v_and_b32_e32 v88, 0xffff0000, v88
	v_mov_b32_e32 v78, 0
	v_mov_b32_e32 v79, 0
	v_mov_b32_e32 v80, 0
	v_mov_b32_e32 v81, 0
	v_cndmask_b32_e32 v90, v90, v7, vcc
	s_cselect_b64 vcc, -1, 0
	s_cmp_eq_u32 s62, 2
	v_med3_f32 v92, v92, s52, v163
	v_med3_f32 v82, v82, s52, v163
	v_med3_f32 v94, v94, s52, v163
	v_med3_f32 v84, v84, s52, v163
	v_med3_f32 v96, v96, s52, v163
	v_med3_f32 v86, v86, s52, v163
	v_med3_f32 v98, v98, s52, v163
	v_med3_f32 v88, v88, s52, v163
	v_cndmask_b32_e32 v100, v2, v1, vcc
	s_cselect_b64 vcc, -1, 0
	s_cmp_eq_u32 s62, 3
	v_cvt_pk_fp8_f32 v78, v92, v82
	v_cvt_pk_fp8_f32 v79, v94, v84
	v_cvt_pk_fp8_f32 v80, v96, v86
	v_cvt_pk_fp8_f32 v81, v98, v88
	v_cndmask_b32_e32 v91, v100, v4, vcc
	s_cselect_b64 vcc, -1, 0
	s_cmp_eq_u32 s62, 4
	v_cndmask_b32_e32 v91, v91, v3, vcc
	s_cselect_b64 vcc, -1, 0
	s_cmp_eq_u32 s62, 5
	v_lshlrev_b32_e32 v93, 16, v83
	v_and_b32_e32 v83, 0xffff0000, v83
	v_lshlrev_b32_e32 v95, 16, v85
	v_and_b32_e32 v85, 0xffff0000, v85
	v_lshlrev_b32_e32 v97, 16, v87
	v_and_b32_e32 v87, 0xffff0000, v87
	v_lshlrev_b32_e32 v99, 16, v89
	v_and_b32_e32 v89, 0xffff0000, v89
	v_cndmask_b32_e32 v91, v91, v6, vcc
	s_cselect_b64 vcc, -1, 0
	s_cmp_eq_u32 s62, 6
	v_med3_f32 v93, v93, s52, v163
	v_med3_f32 v83, v83, s52, v163
	v_med3_f32 v95, v95, s52, v163
	v_med3_f32 v85, v85, s52, v163
	v_med3_f32 v97, v97, s52, v163
	v_med3_f32 v87, v87, s52, v163
	v_med3_f32 v99, v99, s52, v163
	v_med3_f32 v89, v89, s52, v163
	v_cndmask_b32_e32 v91, v91, v5, vcc
	s_cselect_b64 vcc, -1, 0
	s_cmp_eq_u32 s62, 7
	v_cvt_pk_fp8_f32 v78, v93, v83 op_sel:[0,0,1]
	v_cvt_pk_fp8_f32 v79, v95, v85 op_sel:[0,0,1]
	v_cvt_pk_fp8_f32 v80, v97, v87 op_sel:[0,0,1]
	v_cvt_pk_fp8_f32 v81, v99, v89 op_sel:[0,0,1]
	v_cndmask_b32_e32 v91, v91, v8, vcc
	s_cselect_b64 vcc, -1, 0
	s_add_i32 s2, s2, 2
	s_cmp_eq_u32 s2, 8
	v_cndmask_b32_e32 v91, v91, v7, vcc
	global_store_dwordx4 v90, v[74:77], s[6:7] nt
	global_store_dwordx4 v91, v[78:81], s[6:7] nt
	s_cbranch_scc0 .LBB0_289
	s_sleep 40
	s_waitcnt lgkmcnt(0)
	s_add_i32 s61, s61, 1
	s_cmp_eq_u32 s61, 32
	s_cbranch_scc0 .LBB0_286
	s_branch .LBB0_275
